# speedup vs baseline: 1.0082x; 1.0082x over previous
.LBB1_14:
	s_or_b64 exec, exec, s[6:7]
	v_mov_b32_e32 v3, 0
	s_load_dword s6, s[0:1], 0x18
	s_waitcnt lgkmcnt(0)
	s_barrier
	ds_read_b32 v1, v3 offset:26112
	s_movk_i32 s7, 0x194
	v_lshlrev_b32_e32 v2, 2, v0
	v_cmp_gt_u32_e32 vcc, 0x100, v0
	s_mov_b64 s[36:37], vcc
	s_add_u32 s20, s4, 0x1000
	s_addc_u32 s21, s5, 0
	s_add_u32 s22, s4, 0x2000
	s_addc_u32 s23, s5, 0
	s_add_u32 s24, s4, 0x3000
	s_addc_u32 s25, s5, 0
	s_add_u32 s26, s4, 0x4000
	s_addc_u32 s27, s5, 0
	s_add_u32 s28, s4, 0x5000
	s_addc_u32 s29, s5, 0
	s_add_u32 s30, s4, 0x6000
	s_addc_u32 s31, s5, 0
	v_lshrrev_b32_e32 v5, 2, v0
	v_mul_u32_u24_e32 v5, 0x147b, v5
	v_lshrrev_b32_e32 v5, 17, v5
	v_mul_u32_u24_e32 v6, 0x64, v5
	v_sub_u32_e32 v17, v0, v6
	v_lshlrev_b32_e32 v6, 2, v17
	v_mad_u32_u24 v6, v5, s7, v6
	ds_read_b32 v10, v6
	v_add_u32_e32 v4, 0x400, v0
	v_lshrrev_b32_e32 v5, 2, v4
	v_mul_u32_u24_e32 v5, 0x147b, v5
	v_lshrrev_b32_e32 v5, 17, v5
	v_mul_u32_u24_e32 v6, 0x64, v5
	v_sub_u32_e32 v18, v4, v6
	v_lshlrev_b32_e32 v6, 2, v18
	v_mad_u32_u24 v6, v5, s7, v6
	ds_read_b32 v11, v6
	v_add_u32_e32 v4, 0x800, v0
	v_lshrrev_b32_e32 v5, 2, v4
	v_mul_u32_u24_e32 v5, 0x147b, v5
	v_lshrrev_b32_e32 v5, 17, v5
	v_mul_u32_u24_e32 v6, 0x64, v5
	v_sub_u32_e32 v19, v4, v6
	v_lshlrev_b32_e32 v6, 2, v19
	v_mad_u32_u24 v6, v5, s7, v6
	ds_read_b32 v12, v6
	v_add_u32_e32 v4, 0xc00, v0
	v_lshrrev_b32_e32 v5, 2, v4
	v_mul_u32_u24_e32 v5, 0x147b, v5
	v_lshrrev_b32_e32 v5, 17, v5
	v_mul_u32_u24_e32 v6, 0x64, v5
	v_sub_u32_e32 v20, v4, v6
	v_lshlrev_b32_e32 v6, 2, v20
	v_mad_u32_u24 v6, v5, s7, v6
	ds_read_b32 v13, v6
	v_add_u32_e32 v4, 0x1000, v0
	v_lshrrev_b32_e32 v5, 2, v4
	v_mul_u32_u24_e32 v5, 0x147b, v5
	v_lshrrev_b32_e32 v5, 17, v5
	v_mul_u32_u24_e32 v6, 0x64, v5
	v_sub_u32_e32 v21, v4, v6
	v_lshlrev_b32_e32 v6, 2, v21
	v_mad_u32_u24 v6, v5, s7, v6
	ds_read_b32 v14, v6
	v_add_u32_e32 v4, 0x1400, v0
	v_lshrrev_b32_e32 v5, 2, v4
	v_mul_u32_u24_e32 v5, 0x147b, v5
	v_lshrrev_b32_e32 v5, 17, v5
	v_mul_u32_u24_e32 v6, 0x64, v5
	v_sub_u32_e32 v22, v4, v6
	v_lshlrev_b32_e32 v6, 2, v22
	v_mad_u32_u24 v6, v5, s7, v6
	ds_read_b32 v15, v6
	v_add_u32_e32 v4, 0x1800, v0
	v_lshrrev_b32_e32 v5, 2, v4
	v_mul_u32_u24_e32 v5, 0x147b, v5
	v_lshrrev_b32_e32 v5, 17, v5
	v_mul_u32_u24_e32 v6, 0x64, v5
	v_sub_u32_e32 v23, v4, v6
	v_lshlrev_b32_e32 v6, 2, v23
	v_mad_u32_u24 v6, v5, s7, v6
	s_and_saveexec_b64 s[38:39], s[36:37]
	ds_read_b32 v16, v6
	s_mov_b64 exec, s[38:39]
	s_waitcnt lgkmcnt(0)
	v_cmp_ge_i32_e32 vcc, v1, v17
	v_cmp_gt_i32_e64 s[0:1], s6, v17
	s_and_b64 s[0:1], vcc, s[0:1]
	v_cndmask_b32_e64 v10, 0, v10, s[0:1]
	v_cmp_ge_i32_e32 vcc, v1, v18
	v_cmp_gt_i32_e64 s[0:1], s6, v18
	s_and_b64 s[0:1], vcc, s[0:1]
	v_cndmask_b32_e64 v11, 0, v11, s[0:1]
	v_cmp_ge_i32_e32 vcc, v1, v19
	v_cmp_gt_i32_e64 s[0:1], s6, v19
	s_and_b64 s[0:1], vcc, s[0:1]
	v_cndmask_b32_e64 v12, 0, v12, s[0:1]
	v_cmp_ge_i32_e32 vcc, v1, v20
	v_cmp_gt_i32_e64 s[0:1], s6, v20
	s_and_b64 s[0:1], vcc, s[0:1]
	v_cndmask_b32_e64 v13, 0, v13, s[0:1]
	v_cmp_ge_i32_e32 vcc, v1, v21
	v_cmp_gt_i32_e64 s[0:1], s6, v21
	s_and_b64 s[0:1], vcc, s[0:1]
	v_cndmask_b32_e64 v14, 0, v14, s[0:1]
	v_cmp_ge_i32_e32 vcc, v1, v22
	v_cmp_gt_i32_e64 s[0:1], s6, v22
	s_and_b64 s[0:1], vcc, s[0:1]
	v_cndmask_b32_e64 v15, 0, v15, s[0:1]
	v_cmp_ge_i32_e32 vcc, v1, v23
	v_cmp_gt_i32_e64 s[0:1], s6, v23
	s_and_b64 s[0:1], vcc, s[0:1]
	v_cndmask_b32_e64 v16, 0, v16, s[0:1]
	global_store_dword v2, v10, s[4:5]
	global_store_dword v2, v11, s[20:21]
	global_store_dword v2, v12, s[22:23]
	global_store_dword v2, v13, s[24:25]
	global_store_dword v2, v14, s[26:27]
	global_store_dword v2, v15, s[28:29]
	s_and_saveexec_b64 s[38:39], s[36:37]
	global_store_dword v2, v16, s[30:31]
	s_endpgm

	.amdhsa_kernel _Z12final_kernelPKfS0_Pfi
		.amdhsa_group_segment_fixed_size 26116
		.amdhsa_private_segment_fixed_size 0
		.amdhsa_kernarg_size 28
		.amdhsa_user_sgpr_count 2
		.amdhsa_user_sgpr_dispatch_ptr 0
		.amdhsa_user_sgpr_queue_ptr 0
		.amdhsa_user_sgpr_kernarg_segment_ptr 1
		.amdhsa_user_sgpr_dispatch_id 0
		.amdhsa_user_sgpr_kernarg_preload_length 0
		.amdhsa_user_sgpr_kernarg_preload_offset 0
		.amdhsa_user_sgpr_private_segment_size 0
		.amdhsa_uses_dynamic_stack 0
		.amdhsa_enable_private_segment 0
		.amdhsa_system_sgpr_workgroup_id_x 1
		.amdhsa_system_sgpr_workgroup_id_y 0
		.amdhsa_system_sgpr_workgroup_id_z 0
		.amdhsa_system_sgpr_workgroup_info 0
		.amdhsa_system_vgpr_workitem_id 0
		.amdhsa_next_free_vgpr 36
		.amdhsa_next_free_sgpr 40
		.amdhsa_accum_offset 36
		.amdhsa_reserve_vcc 1
		.amdhsa_float_round_mode_32 0
		.amdhsa_float_round_mode_16_64 0
		.amdhsa_float_denorm_mode_32 3
		.amdhsa_float_denorm_mode_16_64 3
		.amdhsa_dx10_clamp 1
		.amdhsa_ieee_mode 1
		.amdhsa_fp16_overflow 0
		.amdhsa_tg_split 0
		.amdhsa_exception_fp_ieee_invalid_op 0
		.amdhsa_exception_fp_denorm_src 0
		.amdhsa_exception_fp_ieee_div_zero 0
		.amdhsa_exception_fp_ieee_overflow 0
		.amdhsa_exception_fp_ieee_underflow 0
		.amdhsa_exception_fp_ieee_inexact 0
		.amdhsa_exception_int_div_zero 0
	.end_amdhsa_kernel

amdhsa.kernels:
  - .agpr_count:     240
    .args:
      - .actual_access:  read_only
        .address_space:  global
        .offset:         0
        .size:           8
        .value_kind:     global_buffer
      - .actual_access:  read_only
        .address_space:  global
        .offset:         8
        .size:           8
        .value_kind:     global_buffer
      - .actual_access:  read_only
        .address_space:  global
        .offset:         16
        .size:           8
        .value_kind:     global_buffer
      - .address_space:  global
        .offset:         24
        .size:           8
        .value_kind:     global_buffer
      - .actual_access:  write_only
        .address_space:  global
        .offset:         32
        .size:           8
        .value_kind:     global_buffer
    .group_segment_fixed_size: 158272
    .kernarg_segment_align: 8
    .kernarg_segment_size: 40
    .language:       OpenCL C
    .language_version:
      - 2
      - 0
    .max_flat_workgroup_size: 256
    .name:           _Z11jacobi_mainPKfS0_S0_PyPf
    .private_segment_fixed_size: 0
    .sgpr_count:     80
    .sgpr_spill_count: 0
    .symbol:         _Z11jacobi_mainPKfS0_S0_PyPf.kd
    .uniform_work_group_size: 1
    .uses_dynamic_stack: false
    .vgpr_count:     496
    .vgpr_spill_count: 0
    .wavefront_size: 64
  - .agpr_count:     0
    .args:
      - .actual_access:  read_only
        .address_space:  global
        .offset:         0
        .size:           8
        .value_kind:     global_buffer
      - .actual_access:  read_only
        .address_space:  global
        .offset:         8
        .size:           8
        .value_kind:     global_buffer
      - .actual_access:  write_only
        .address_space:  global
        .offset:         16
        .size:           8
        .value_kind:     global_buffer
      - .offset:         24
        .size:           4
        .value_kind:     by_value
    .group_segment_fixed_size: 26116
    .kernarg_segment_align: 8
    .kernarg_segment_size: 28
    .language:       OpenCL C
    .language_version:
      - 2
      - 0
    .max_flat_workgroup_size: 1024
    .name:           _Z12final_kernelPKfS0_Pfi
    .private_segment_fixed_size: 0
    .sgpr_count:     46
    .sgpr_spill_count: 0
    .symbol:         _Z12final_kernelPKfS0_Pfi.kd
    .uniform_work_group_size: 1
    .uses_dynamic_stack: false
    .vgpr_count:     36
    .vgpr_spill_count: 0
    .wavefront_size: 64
